# GDN section c: the ten non-zero LM tiles spread over all eight waves (max two per wave); qk tiles run in section d; never-read upper LM tiles not written
# speedup vs baseline: 1.0025x; 1.0025x over previous
.Lgpf_done_next:
	v_and_b32_e32 v0, 15, v215
	v_lshrrev_b32_e32 v1, 4, v215
	v_mul_u32_u24_e32 v4, 0x110, v0
	v_lshl_add_u32 v4, v1, 4, v4
	v_lshlrev_b32_e32 v5, 4, v1
	v_lshlrev_b32_e32 v6, 2, v0
	v_add_u32_e32 v6, 0x1c400, v6
	s_mov_b32 s34, 0x3fb8aa3b
	s_cmp_eq_u32 s10, 16
	s_cbranch_scc1 .Lgc_w1
	s_cmp_eq_u32 s10, 32
	s_cbranch_scc1 .Lgc_w2
	s_cmp_eq_u32 s10, 48
	s_cbranch_scc1 .Lgc_w3
	s_cmp_eq_u32 s10, 64
	s_cbranch_scc1 .Lgc_w4
	s_cmp_eq_u32 s10, 80
	s_cbranch_scc1 .Lgc_w5
	s_cmp_eq_u32 s10, 96
	s_cbranch_scc1 .Lgc_w6
	s_cmp_eq_u32 s10, 112
	s_cbranch_scc1 .Lgc_join
	v_add_u32_e32 v3, 0x4400, v4
	v_add_u32_e32 v5, 0x1c400, v5
	ds_read_b128 v[40:43], v3
	ds_read_b128 v[44:47], v3 offset:64
	ds_read_b128 v[48:51], v3 offset:128
	ds_read_b128 v[52:55], v3 offset:192
	ds_read_b128 v[56:59], v4
	ds_read_b128 v[60:63], v4 offset:64
	ds_read_b128 v[64:67], v4 offset:128
	ds_read_b128 v[68:71], v4 offset:192
	ds_read_b128 v[144:147], v5
	ds_read_b32 v136, v6
	v_lshl_add_u32 v12, v1, 2, 0
	v_add_u32_e32 v13, 1, v12
	v_add_u32_e32 v14, 2, v12
	v_add_u32_e32 v15, 3, v12
	s_waitcnt lgkmcnt(0)
	v_mfma_f32_16x16x32_bf16 v[120:123], v[40:43], v[56:59], 0
	v_mfma_f32_16x16x32_bf16 v[120:123], v[44:47], v[60:63], v[120:123]
	v_mfma_f32_16x16x32_bf16 v[120:123], v[48:51], v[64:67], v[120:123]
	v_mfma_f32_16x16x32_bf16 v[120:123], v[52:55], v[68:71], v[120:123]
	v_sub_f32_e32 v148, v144, v136
	v_sub_f32_e32 v149, v145, v136
	v_sub_f32_e32 v150, v146, v136
	v_sub_f32_e32 v151, v147, v136
	v_mul_f32_e32 v148, s34, v148
	v_mul_f32_e32 v149, s34, v149
	v_mul_f32_e32 v150, s34, v150
	v_mul_f32_e32 v151, s34, v151
	v_exp_f32_e32 v148, v148
	v_exp_f32_e32 v149, v149
	v_exp_f32_e32 v150, v150
	v_exp_f32_e32 v151, v151
	v_mul_f32_e32 v148, v120, v148
	v_mul_f32_e32 v149, v121, v149
	v_mul_f32_e32 v150, v122, v150
	v_mul_f32_e32 v151, v123, v151
	v_cmp_lt_i32_e32 vcc, v0, v12
	v_cmp_lt_i32_e64 s[0:1], v0, v13
	v_cmp_lt_i32_e64 s[20:21], v0, v14
	v_cndmask_b32_e32 v148, 0, v148, vcc
	v_cmp_lt_i32_e32 vcc, v0, v15
	v_cndmask_b32_e64 v149, 0, v149, s[0:1]
	v_cndmask_b32_e64 v150, 0, v150, s[20:21]
	s_nop 0
	v_cndmask_b32_e32 v151, 0, v151, vcc
	v_add_u32_e32 v16, 0x15c00, v4
	ds_write_b128 v16, v[148:151]
	s_branch .Lgc_join
.Lgc_w1:
	v_add_u32_e32 v3, 0x5500, v4
	v_add_u32_e32 v5, 0x1c440, v5
	ds_read_b128 v[40:43], v3
	ds_read_b128 v[44:47], v3 offset:64
	ds_read_b128 v[48:51], v3 offset:128
	ds_read_b128 v[52:55], v3 offset:192
	ds_read_b128 v[56:59], v4
	ds_read_b128 v[60:63], v4 offset:64
	ds_read_b128 v[64:67], v4 offset:128
	ds_read_b128 v[68:71], v4 offset:192
	ds_read_b128 v[144:147], v5
	ds_read_b32 v136, v6
	ds_read_b32 v137, v6 offset:64
	ds_read_b128 v[72:75], v4 offset:4352
	ds_read_b128 v[76:79], v4 offset:4416
	ds_read_b128 v[80:83], v4 offset:4480
	ds_read_b128 v[84:87], v4 offset:4544
	v_add_u32_e32 v9, 16, v0
	v_lshl_add_u32 v12, v1, 2, 16
	v_add_u32_e32 v13, 1, v12
	v_add_u32_e32 v14, 2, v12
	v_add_u32_e32 v15, 3, v12
	s_waitcnt lgkmcnt(5)
	v_mfma_f32_16x16x32_bf16 v[120:123], v[40:43], v[56:59], 0
	v_mfma_f32_16x16x32_bf16 v[120:123], v[44:47], v[60:63], v[120:123]
	v_mfma_f32_16x16x32_bf16 v[120:123], v[48:51], v[64:67], v[120:123]
	v_mfma_f32_16x16x32_bf16 v[120:123], v[52:55], v[68:71], v[120:123]
	v_sub_f32_e32 v148, v144, v136
	v_sub_f32_e32 v149, v145, v136
	v_sub_f32_e32 v150, v146, v136
	v_sub_f32_e32 v151, v147, v136
	v_mul_f32_e32 v148, s34, v148
	v_mul_f32_e32 v149, s34, v149
	v_mul_f32_e32 v150, s34, v150
	v_mul_f32_e32 v151, s34, v151
	v_exp_f32_e32 v148, v148
	v_exp_f32_e32 v149, v149
	v_exp_f32_e32 v150, v150
	v_exp_f32_e32 v151, v151
	s_waitcnt lgkmcnt(0)
	v_mfma_f32_16x16x32_bf16 v[124:127], v[40:43], v[72:75], 0
	v_mfma_f32_16x16x32_bf16 v[124:127], v[44:47], v[76:79], v[124:127]
	v_mfma_f32_16x16x32_bf16 v[124:127], v[48:51], v[80:83], v[124:127]
	v_mfma_f32_16x16x32_bf16 v[124:127], v[52:55], v[84:87], v[124:127]
	v_mul_f32_e32 v148, v120, v148
	v_mul_f32_e32 v149, v121, v149
	v_mul_f32_e32 v150, v122, v150
	v_mul_f32_e32 v151, v123, v151
	v_sub_f32_e32 v152, v144, v137
	v_sub_f32_e32 v153, v145, v137
	v_sub_f32_e32 v154, v146, v137
	v_sub_f32_e32 v155, v147, v137
	v_mul_f32_e32 v152, s34, v152
	v_mul_f32_e32 v153, s34, v153
	v_mul_f32_e32 v154, s34, v154
	v_mul_f32_e32 v155, s34, v155
	v_exp_f32_e32 v152, v152
	v_exp_f32_e32 v153, v153
	v_exp_f32_e32 v154, v154
	v_exp_f32_e32 v155, v155
	v_mul_f32_e32 v152, v124, v152
	v_mul_f32_e32 v153, v125, v153
	v_mul_f32_e32 v154, v126, v154
	v_mul_f32_e32 v155, v127, v155
	v_cmp_lt_i32_e32 vcc, v9, v12
	v_cmp_lt_i32_e64 s[0:1], v9, v13
	v_cmp_lt_i32_e64 s[20:21], v9, v14
	v_cndmask_b32_e32 v152, 0, v152, vcc
	v_cmp_lt_i32_e32 vcc, v9, v15
	v_cndmask_b32_e64 v153, 0, v153, s[0:1]
	v_cndmask_b32_e64 v154, 0, v154, s[20:21]
	s_nop 0
	v_cndmask_b32_e32 v155, 0, v155, vcc
	v_add_u32_e32 v16, 0x15c40, v4
	ds_write_b128 v16, v[148:151]
	ds_write_b128 v16, v[152:155] offset:4352
	s_branch .Lgc_join
.Lgc_w2:
	v_add_u32_e32 v3, 0x6600, v4
	v_add_u32_e32 v5, 0x1c480, v5
	ds_read_b128 v[40:43], v3
	ds_read_b128 v[44:47], v3 offset:64
	ds_read_b128 v[48:51], v3 offset:128
	ds_read_b128 v[52:55], v3 offset:192
	ds_read_b128 v[56:59], v4
	ds_read_b128 v[60:63], v4 offset:64
	ds_read_b128 v[64:67], v4 offset:128
	ds_read_b128 v[68:71], v4 offset:192
	ds_read_b128 v[144:147], v5
	ds_read_b32 v136, v6
	ds_read_b32 v137, v6 offset:64
	ds_read_b128 v[72:75], v4 offset:4352
	ds_read_b128 v[76:79], v4 offset:4416
	ds_read_b128 v[80:83], v4 offset:4480
	ds_read_b128 v[84:87], v4 offset:4544
	s_waitcnt lgkmcnt(5)
	v_mfma_f32_16x16x32_bf16 v[120:123], v[40:43], v[56:59], 0
	v_mfma_f32_16x16x32_bf16 v[120:123], v[44:47], v[60:63], v[120:123]
	v_mfma_f32_16x16x32_bf16 v[120:123], v[48:51], v[64:67], v[120:123]
	v_mfma_f32_16x16x32_bf16 v[120:123], v[52:55], v[68:71], v[120:123]
	v_sub_f32_e32 v148, v144, v136
	v_sub_f32_e32 v149, v145, v136
	v_sub_f32_e32 v150, v146, v136
	v_sub_f32_e32 v151, v147, v136
	v_mul_f32_e32 v148, s34, v148
	v_mul_f32_e32 v149, s34, v149
	v_mul_f32_e32 v150, s34, v150
	v_mul_f32_e32 v151, s34, v151
	v_exp_f32_e32 v148, v148
	v_exp_f32_e32 v149, v149
	v_exp_f32_e32 v150, v150
	v_exp_f32_e32 v151, v151
	s_waitcnt lgkmcnt(0)
	v_mfma_f32_16x16x32_bf16 v[124:127], v[40:43], v[72:75], 0
	v_mfma_f32_16x16x32_bf16 v[124:127], v[44:47], v[76:79], v[124:127]
	v_mfma_f32_16x16x32_bf16 v[124:127], v[48:51], v[80:83], v[124:127]
	v_mfma_f32_16x16x32_bf16 v[124:127], v[52:55], v[84:87], v[124:127]
	v_mul_f32_e32 v148, v120, v148
	v_mul_f32_e32 v149, v121, v149
	v_mul_f32_e32 v150, v122, v150
	v_mul_f32_e32 v151, v123, v151
	v_sub_f32_e32 v152, v144, v137
	v_sub_f32_e32 v153, v145, v137
	v_sub_f32_e32 v154, v146, v137
	v_sub_f32_e32 v155, v147, v137
	v_mul_f32_e32 v152, s34, v152
	v_mul_f32_e32 v153, s34, v153
	v_mul_f32_e32 v154, s34, v154
	v_mul_f32_e32 v155, s34, v155
	v_exp_f32_e32 v152, v152
	v_exp_f32_e32 v153, v153
	v_exp_f32_e32 v154, v154
	v_exp_f32_e32 v155, v155
	v_mul_f32_e32 v152, v124, v152
	v_mul_f32_e32 v153, v125, v153
	v_mul_f32_e32 v154, v126, v154
	v_mul_f32_e32 v155, v127, v155
	v_add_u32_e32 v16, 0x15c80, v4
	ds_write_b128 v16, v[148:151]
	ds_write_b128 v16, v[152:155] offset:4352
	v_mul_u32_u24_e32 v17, 0x140, v1
	v_lshl_add_u32 v17, v0, 1, v17
	v_add_u32_e32 v17, 0x1c800, v17
	v_cvt_pk_bf16_f32 v164, v148, v148
	v_cvt_pk_bf16_f32 v165, v149, v149
	v_cvt_pk_bf16_f32 v166, v150, v150
	v_cvt_pk_bf16_f32 v167, v151, v151
	v_cvt_pk_bf16_f32 v168, v152, v152
	v_cvt_pk_bf16_f32 v169, v153, v153
	v_cvt_pk_bf16_f32 v170, v154, v154
	v_cvt_pk_bf16_f32 v171, v155, v155
	ds_write_b16 v17, v164
	ds_write_b16 v17, v165 offset:80
	ds_write_b16 v17, v166 offset:160
	ds_write_b16 v17, v167 offset:240
	ds_write_b16 v17, v168 offset:32
	ds_write_b16 v17, v169 offset:112
	ds_write_b16 v17, v170 offset:192
	ds_write_b16 v17, v171 offset:272
	s_branch .Lgc_join
.Lgc_w3:
	v_add_u32_e32 v3, 0x7700, v4
	v_add_u32_e32 v5, 0x1c4c0, v5
	ds_read_b128 v[40:43], v3
	ds_read_b128 v[44:47], v3 offset:64
	ds_read_b128 v[48:51], v3 offset:128
	ds_read_b128 v[52:55], v3 offset:192
	ds_read_b128 v[56:59], v4
	ds_read_b128 v[60:63], v4 offset:64
	ds_read_b128 v[64:67], v4 offset:128
	ds_read_b128 v[68:71], v4 offset:192
	ds_read_b128 v[144:147], v5
	ds_read_b32 v136, v6
	ds_read_b32 v137, v6 offset:64
	ds_read_b128 v[72:75], v4 offset:4352
	ds_read_b128 v[76:79], v4 offset:4416
	ds_read_b128 v[80:83], v4 offset:4480
	ds_read_b128 v[84:87], v4 offset:4544
	s_waitcnt lgkmcnt(5)
	v_mfma_f32_16x16x32_bf16 v[120:123], v[40:43], v[56:59], 0
	v_mfma_f32_16x16x32_bf16 v[120:123], v[44:47], v[60:63], v[120:123]
	v_mfma_f32_16x16x32_bf16 v[120:123], v[48:51], v[64:67], v[120:123]
	v_mfma_f32_16x16x32_bf16 v[120:123], v[52:55], v[68:71], v[120:123]
	v_sub_f32_e32 v148, v144, v136
	v_sub_f32_e32 v149, v145, v136
	v_sub_f32_e32 v150, v146, v136
	v_sub_f32_e32 v151, v147, v136
	v_mul_f32_e32 v148, s34, v148
	v_mul_f32_e32 v149, s34, v149
	v_mul_f32_e32 v150, s34, v150
	v_mul_f32_e32 v151, s34, v151
	v_exp_f32_e32 v148, v148
	v_exp_f32_e32 v149, v149
	v_exp_f32_e32 v150, v150
	v_exp_f32_e32 v151, v151
	s_waitcnt lgkmcnt(0)
	v_mfma_f32_16x16x32_bf16 v[124:127], v[40:43], v[72:75], 0
	v_mfma_f32_16x16x32_bf16 v[124:127], v[44:47], v[76:79], v[124:127]
	v_mfma_f32_16x16x32_bf16 v[124:127], v[48:51], v[80:83], v[124:127]
	v_mfma_f32_16x16x32_bf16 v[124:127], v[52:55], v[84:87], v[124:127]
	v_mul_f32_e32 v148, v120, v148
	v_mul_f32_e32 v149, v121, v149
	v_mul_f32_e32 v150, v122, v150
	v_mul_f32_e32 v151, v123, v151
	v_sub_f32_e32 v152, v144, v137
	v_sub_f32_e32 v153, v145, v137
	v_sub_f32_e32 v154, v146, v137
	v_sub_f32_e32 v155, v147, v137
	v_mul_f32_e32 v152, s34, v152
	v_mul_f32_e32 v153, s34, v153
	v_mul_f32_e32 v154, s34, v154
	v_mul_f32_e32 v155, s34, v155
	v_exp_f32_e32 v152, v152
	v_exp_f32_e32 v153, v153
	v_exp_f32_e32 v154, v154
	v_exp_f32_e32 v155, v155
	v_mul_f32_e32 v152, v124, v152
	v_mul_f32_e32 v153, v125, v153
	v_mul_f32_e32 v154, v126, v154
	v_mul_f32_e32 v155, v127, v155
	v_add_u32_e32 v16, 0x15cc0, v4
	ds_write_b128 v16, v[148:151]
	ds_write_b128 v16, v[152:155] offset:4352
	v_mul_u32_u24_e32 v17, 0x140, v1
	v_lshl_add_u32 v17, v0, 1, v17
	v_add_u32_e32 v17, 0x1cd00, v17
	v_cvt_pk_bf16_f32 v164, v148, v148
	v_cvt_pk_bf16_f32 v165, v149, v149
	v_cvt_pk_bf16_f32 v166, v150, v150
	v_cvt_pk_bf16_f32 v167, v151, v151
	v_cvt_pk_bf16_f32 v168, v152, v152
	v_cvt_pk_bf16_f32 v169, v153, v153
	v_cvt_pk_bf16_f32 v170, v154, v154
	v_cvt_pk_bf16_f32 v171, v155, v155
	ds_write_b16 v17, v164
	ds_write_b16 v17, v165 offset:80
	ds_write_b16 v17, v166 offset:160
	ds_write_b16 v17, v167 offset:240
	ds_write_b16 v17, v168 offset:32
	ds_write_b16 v17, v169 offset:112
	ds_write_b16 v17, v170 offset:192
	ds_write_b16 v17, v171 offset:272
	s_branch .Lgc_join
.Lgc_w4:
	v_add_u32_e32 v3, 0x6600, v4
	v_add_u32_e32 v5, 0x1c480, v5
	ds_read_b128 v[40:43], v3
	ds_read_b128 v[44:47], v3 offset:64
	ds_read_b128 v[48:51], v3 offset:128
	ds_read_b128 v[52:55], v3 offset:192
	ds_read_b128 v[88:91], v4 offset:8704
	ds_read_b128 v[92:95], v4 offset:8768
	ds_read_b128 v[96:99], v4 offset:8832
	ds_read_b128 v[100:103], v4 offset:8896
	ds_read_b128 v[144:147], v5
	ds_read_b32 v138, v6 offset:128
	v_add_u32_e32 v10, 32, v0
	v_lshl_add_u32 v12, v1, 2, 32
	v_add_u32_e32 v13, 1, v12
	v_add_u32_e32 v14, 2, v12
	v_add_u32_e32 v15, 3, v12
	s_waitcnt lgkmcnt(0)
	v_mfma_f32_16x16x32_bf16 v[128:131], v[40:43], v[88:91], 0
	v_mfma_f32_16x16x32_bf16 v[128:131], v[44:47], v[92:95], v[128:131]
	v_mfma_f32_16x16x32_bf16 v[128:131], v[48:51], v[96:99], v[128:131]
	v_mfma_f32_16x16x32_bf16 v[128:131], v[52:55], v[100:103], v[128:131]
	v_sub_f32_e32 v156, v144, v138
	v_sub_f32_e32 v157, v145, v138
	v_sub_f32_e32 v158, v146, v138
	v_sub_f32_e32 v159, v147, v138
	v_mul_f32_e32 v156, s34, v156
	v_mul_f32_e32 v157, s34, v157
	v_mul_f32_e32 v158, s34, v158
	v_mul_f32_e32 v159, s34, v159
	v_exp_f32_e32 v156, v156
	v_exp_f32_e32 v157, v157
	v_exp_f32_e32 v158, v158
	v_exp_f32_e32 v159, v159
	v_mul_f32_e32 v156, v128, v156
	v_mul_f32_e32 v157, v129, v157
	v_mul_f32_e32 v158, v130, v158
	v_mul_f32_e32 v159, v131, v159
	v_cmp_lt_i32_e32 vcc, v10, v12
	v_cmp_lt_i32_e64 s[0:1], v10, v13
	v_cmp_lt_i32_e64 s[20:21], v10, v14
	v_cndmask_b32_e32 v156, 0, v156, vcc
	v_cmp_lt_i32_e32 vcc, v10, v15
	v_cndmask_b32_e64 v157, 0, v157, s[0:1]
	v_cndmask_b32_e64 v158, 0, v158, s[20:21]
	s_nop 0
	v_cndmask_b32_e32 v159, 0, v159, vcc
	v_add_u32_e32 v16, 0x15c80, v4
	ds_write_b128 v16, v[156:159] offset:8704
	s_branch .Lgc_join
.Lgc_w5:
	v_add_u32_e32 v3, 0x7700, v4
	v_add_u32_e32 v5, 0x1c4c0, v5
	ds_read_b128 v[40:43], v3
	ds_read_b128 v[44:47], v3 offset:64
	ds_read_b128 v[48:51], v3 offset:128
	ds_read_b128 v[52:55], v3 offset:192
	ds_read_b128 v[88:91], v4 offset:8704
	ds_read_b128 v[92:95], v4 offset:8768
	ds_read_b128 v[96:99], v4 offset:8832
	ds_read_b128 v[100:103], v4 offset:8896
	ds_read_b128 v[144:147], v5
	ds_read_b32 v138, v6 offset:128
	s_waitcnt lgkmcnt(0)
	v_mfma_f32_16x16x32_bf16 v[128:131], v[40:43], v[88:91], 0
	v_mfma_f32_16x16x32_bf16 v[128:131], v[44:47], v[92:95], v[128:131]
	v_mfma_f32_16x16x32_bf16 v[128:131], v[48:51], v[96:99], v[128:131]
	v_mfma_f32_16x16x32_bf16 v[128:131], v[52:55], v[100:103], v[128:131]
	v_sub_f32_e32 v156, v144, v138
	v_sub_f32_e32 v157, v145, v138
	v_sub_f32_e32 v158, v146, v138
	v_sub_f32_e32 v159, v147, v138
	v_mul_f32_e32 v156, s34, v156
	v_mul_f32_e32 v157, s34, v157
	v_mul_f32_e32 v158, s34, v158
	v_mul_f32_e32 v159, s34, v159
	v_exp_f32_e32 v156, v156
	v_exp_f32_e32 v157, v157
	v_exp_f32_e32 v158, v158
	v_exp_f32_e32 v159, v159
	v_mul_f32_e32 v156, v128, v156
	v_mul_f32_e32 v157, v129, v157
	v_mul_f32_e32 v158, v130, v158
	v_mul_f32_e32 v159, v131, v159
	v_add_u32_e32 v16, 0x15cc0, v4
	ds_write_b128 v16, v[156:159] offset:8704
	s_branch .Lgc_join
.Lgc_w6:
	v_add_u32_e32 v3, 0x7700, v4
	v_add_u32_e32 v5, 0x1c4c0, v5
	ds_read_b128 v[40:43], v3
	ds_read_b128 v[44:47], v3 offset:64
	ds_read_b128 v[48:51], v3 offset:128
	ds_read_b128 v[52:55], v3 offset:192
	ds_read_b128 v[104:107], v4 offset:13056
	ds_read_b128 v[108:111], v4 offset:13120
	ds_read_b128 v[112:115], v4 offset:13184
	ds_read_b128 v[116:119], v4 offset:13248
	ds_read_b128 v[144:147], v5
	ds_read_b32 v139, v6 offset:192
	v_add_u32_e32 v11, 48, v0
	v_lshl_add_u32 v12, v1, 2, 48
	v_add_u32_e32 v13, 1, v12
	v_add_u32_e32 v14, 2, v12
	v_add_u32_e32 v15, 3, v12
	s_waitcnt lgkmcnt(0)
	v_mfma_f32_16x16x32_bf16 v[132:135], v[40:43], v[104:107], 0
	v_mfma_f32_16x16x32_bf16 v[132:135], v[44:47], v[108:111], v[132:135]
	v_mfma_f32_16x16x32_bf16 v[132:135], v[48:51], v[112:115], v[132:135]
	v_mfma_f32_16x16x32_bf16 v[132:135], v[52:55], v[116:119], v[132:135]
	v_sub_f32_e32 v160, v144, v139
	v_sub_f32_e32 v161, v145, v139
	v_sub_f32_e32 v162, v146, v139
	v_sub_f32_e32 v163, v147, v139
	v_mul_f32_e32 v160, s34, v160
	v_mul_f32_e32 v161, s34, v161
	v_mul_f32_e32 v162, s34, v162
	v_mul_f32_e32 v163, s34, v163
	v_exp_f32_e32 v160, v160
	v_exp_f32_e32 v161, v161
	v_exp_f32_e32 v162, v162
	v_exp_f32_e32 v163, v163
	v_mul_f32_e32 v160, v132, v160
	v_mul_f32_e32 v161, v133, v161
	v_mul_f32_e32 v162, v134, v162
	v_mul_f32_e32 v163, v135, v163
	v_cmp_lt_i32_e32 vcc, v11, v12
	v_cmp_lt_i32_e64 s[0:1], v11, v13
	v_cmp_lt_i32_e64 s[20:21], v11, v14
	v_cndmask_b32_e32 v160, 0, v160, vcc
	v_cmp_lt_i32_e32 vcc, v11, v15
	v_cndmask_b32_e64 v161, 0, v161, s[0:1]
	v_cndmask_b32_e64 v162, 0, v162, s[20:21]
	s_nop 0
	v_cndmask_b32_e32 v163, 0, v163, vcc
	v_add_u32_e32 v16, 0x15cc0, v4
	ds_write_b128 v16, v[160:163] offset:13056
	s_branch .Lgc_join
